# in-projection forget-gate block: bias loaded at the start of the tile-13 epilogue, counted vmcnt(6) instead of vmcnt(0) before its use
# baseline (speedup 1.0000x reference)
; #define PG8_PACK8(y0, y1) (u32x4){cvt_pk_bf16((y0)[0], (y0)[1]), cvt_pk_bf16((y0)[2], (y0)[3]), cvt_pk_bf16((y1)[0], (y1)[1]), cvt_pk_bf16((y1)[2], (y1)[3])}
;     __device__ __forceinline__ void operator()(const f32x4 (&acc)[2][2][4][2], const Unit& u, int ui, int wr, int wc, int fr, int fq) const {
;     ...
;         } else if (pn < 12) {
;             unsigned char* dst = ws + E_QKVO + (size_t)((unsigned)(u.pm >> 4) * (24u << 20) + (16u << 20) + (unsigned)(((pn & 3) * 256 + wc * 64 + 8 * fq) * 2));
; #pragma unroll
;             for (int ai = 0; ai < 2; ++ai)
; #pragma unroll
;                 for (int m = 0; m < 4; ++m) {
;                     const unsigned row = row0 + ai * HALF + m * 16; const float rs = rsp[ai * HALF + m * 16];
; #pragma unroll
;                     for (int bj = 0; bj < 2; ++bj) { const f32x4 y0 = acc[ai][bj][m][0] * rs, y1 = acc[ai][bj][m][1] * rs;
;                         *(u32x4*)(dst + (size_t)(row * 2048u + 64u * bj)) = PG8_PACK8(y0, y1); }
;                 }
;         } else {
; #pragma unroll
;             for (int ai = 0; ai < 2; ++ai)
; #pragma unroll
;                 for (int m = 0; m < 4; ++m) {
;                     const unsigned row = row0 + ai * HALF + m * 16; const float rs = rsp[ai * HALF + m * 16];
; #pragma unroll
;                     for (int bj = 0; bj < 2; ++bj) {
;                         const f32x4 y0 = acc[ai][bj][m][0] * rs, y1 = acc[ai][bj][m][1] * rs;
;                         if (pn == 12 || bj == 0) {
;                             const unsigned gcol = (unsigned)((pn == 12 ? 0 : 256) + 128 * bj + 32 * wc + 8 * fq);
;                             f32x4 s0, s1;
; #pragma unroll
;                             for (int e = 0; e < 4; ++e) { s0[e] = __builtin_amdgcn_rcpf(1.0f + __builtin_amdgcn_exp2f(y0[e] * -1.4426950408889634f)); s1[e] = __builtin_amdgcn_rcpf(1.0f + __builtin_amdgcn_exp2f(y1[e] * -1.4426950408889634f)); }
;                             *(u32x4*)(ws + E_GF + (size_t)((row * 384u + gcol) * 2u)) = PG8_PACK8(s0, s1);
.LBB0_559:
	s_cmp_eq_u32 s4, s42
	s_cselect_b32 s19, 0, 0x400
	v_lshl_add_u32 v158, s4, 8, v163
	v_add_u32_e32 v160, s19, v181
	s_cmp_gt_i32 s26, 7
	s_mov_b64 s[28:29], -1
	s_cbranch_scc0 .LBB0_613
	s_cmp_lt_u32 s26, 12
	s_cbranch_scc1 .LBB0_610
	ds_read_b32 v140, v160
	s_cmp_lg_u32 s26, 12
	s_cselect_b64 s[28:29], -1, 0
	s_cmp_eq_u32 s26, 12
	s_cselect_b32 s19, 0, 0x100
	s_waitcnt lgkmcnt(0)
	v_pk_mul_f32 v[130:131], v[124:125], v[140:141] op_sel_hi:[1,0]
	v_pk_mul_f32 v[134:135], v[126:127], v[140:141] op_sel_hi:[1,0]
	v_pk_mul_f32 v[136:137], v[128:129], v[140:141] op_sel_hi:[1,0]
	v_mul_f32_e32 v130, 0xbfb8aa3b, v130
	v_mul_f32_e32 v0, 0xbfb8aa3b, v134
	v_mul_f32_e32 v134, 0xbfb8aa3b, v135
	v_mul_f32_e32 v135, 0xbfb8aa3b, v136
	v_exp_f32_e32 v130, v130
	v_mul_f32_e32 v136, 0xbfb8aa3b, v137
	v_pk_mul_f32 v[132:133], v[122:123], v[140:141] op_sel_hi:[1,0]
	v_exp_f32_e32 v0, v0
	v_exp_f32_e32 v136, v136
	v_mul_f32_e32 v131, 0xbfb8aa3b, v131
	v_mul_f32_e32 v132, 0xbfb8aa3b, v132
	v_exp_f32_e32 v134, v134
	v_mul_f32_e32 v133, 0xbfb8aa3b, v133
	v_exp_f32_e32 v135, v135
	v_exp_f32_e32 v131, v131
	v_exp_f32_e32 v132, v132
	v_exp_f32_e32 v133, v133
	v_add_f32_e32 v130, 1.0, v130
	v_or_b32_e32 v161, s19, v237
	s_movk_i32 s19, 0x180
	v_add_f32_e32 v0, 1.0, v0
	v_rcp_f32_e32 v137, v130
	v_add_f32_e32 v130, 1.0, v136
	v_mul_lo_u32 v144, v158, s19
	v_rcp_f32_e32 v0, v0
	v_add_f32_e32 v134, 1.0, v134
	v_add_f32_e32 v135, 1.0, v135
	v_rcp_f32_e32 v136, v130
	v_add_f32_e32 v130, 1.0, v131
	v_add_f32_e32 v132, 1.0, v132
	v_rcp_f32_e32 v134, v134
	v_add_f32_e32 v133, 1.0, v133
	v_rcp_f32_e32 v135, v135
	v_rcp_f32_e32 v138, v130
	v_cvt_pk_bf16_f32 v130, v0, v134
	v_add_lshl_u32 v0, v144, v161, 1
	v_rcp_f32_e32 v132, v132
	v_rcp_f32_e32 v133, v133
	v_cvt_pk_bf16_f32 v131, v135, v136
	v_lshl_add_u64 v[134:135], s[10:11], 0, v[0:1]
	v_cvt_pk_bf16_f32 v132, v132, v133
	v_cvt_pk_bf16_f32 v133, v137, v138
	flat_store_dwordx4 v[134:135], v[130:133]
	v_pk_mul_f32 v[134:135], v[120:121], v[140:141] op_sel_hi:[1,0]
	v_pk_mul_f32 v[138:139], v[118:119], v[140:141] op_sel_hi:[1,0]
	v_pk_mul_f32 v[136:137], v[116:117], v[140:141] op_sel_hi:[1,0]
	v_pk_mul_f32 v[140:141], v[114:115], v[140:141] op_sel_hi:[1,0]
	s_mov_b64 s[30:31], -1
	s_and_b64 vcc, exec, s[28:29]
	s_cbranch_vccz .LBB0_565
	global_load_dwordx2 v[116:117], v1, s[6:7]
	global_load_dwordx2 v[100:101], v1, s[6:7] offset:8
	global_load_dwordx2 v[84:85], v1, s[6:7] offset:16
	s_and_saveexec_b64 s[30:31], s[34:35]
	s_cbranch_execz .LBB0_564

; #define PG8_PACK8(y0, y1) (u32x4){cvt_pk_bf16((y0)[0], (y0)[1]), cvt_pk_bf16((y0)[2], (y0)[3]), cvt_pk_bf16((y1)[0], (y1)[1]), cvt_pk_bf16((y1)[2], (y1)[3])}
;     __device__ __forceinline__ void operator()(const f32x4 (&acc)[2][2][4][2], const Unit& u, int ui, int wr, int wc, int fr, int fq) const {
;     ...
;                     const unsigned row = row0 + ai * HALF + m * 16; const float rs = rsp[ai * HALF + m * 16];
; #pragma unroll
;                     for (int bj = 0; bj < 2; ++bj) {
;                         const f32x4 y0 = acc[ai][bj][m][0] * rs, y1 = acc[ai][bj][m][1] * rs;
;                         if (pn == 12 || bj == 0) {
;                             const unsigned gcol = (unsigned)((pn == 12 ? 0 : 256) + 128 * bj + 32 * wc + 8 * fq);
;                             f32x4 s0, s1;
; #pragma unroll
;                             for (int e = 0; e < 4; ++e) { s0[e] = __builtin_amdgcn_rcpf(1.0f + __builtin_amdgcn_exp2f(y0[e] * -1.4426950408889634f)); s1[e] = __builtin_amdgcn_rcpf(1.0f + __builtin_amdgcn_exp2f(y1[e] * -1.4426950408889634f)); }
;                             *(u32x4*)(ws + E_GF + (size_t)((row * 384u + gcol) * 2u)) = PG8_PACK8(s0, s1);
;                         } else if (wc == 0 && fq == 0) {
;                             float z[6] = {y0[0], y0[1], y0[2], y0[3], y1[0], y1[1]};
; #pragma unroll
;                             for (int e = 0; e < 6; ++e) { const float zz = z[e] + bfg[e]; z[e] = fminf(zz, 0.f) - log1pf(__expf(-fabsf(zz))); }
.LBB0_603:
	ds_read_b32 v140, v160 offset:704
	v_add_u32_e32 v0, v159, v161
	s_and_b64 vcc, exec, s[40:41]
	s_mov_b64 s[28:29], -1
	s_waitcnt lgkmcnt(0)
	v_pk_mul_f32 v[130:131], v[10:11], v[140:141] op_sel_hi:[1,0]
	v_pk_mul_f32 v[132:133], v[14:15], v[140:141] op_sel_hi:[1,0]
	v_mul_f32_e32 v130, 0xbfb8aa3b, v130
	v_exp_f32_e32 v130, v130
	v_mul_f32_e32 v133, 0xbfb8aa3b, v133
	v_exp_f32_e32 v133, v133
	v_pk_mul_f32 v[134:135], v[12:13], v[140:141] op_sel_hi:[1,0]
	v_pk_mul_f32 v[136:137], v[16:17], v[140:141] op_sel_hi:[1,0]
	v_add_f32_e32 v130, 1.0, v130
	v_mul_f32_e32 v131, 0xbfb8aa3b, v131
	v_exp_f32_e32 v131, v131
	v_rcp_f32_e32 v138, v130
	v_add_f32_e32 v130, 1.0, v133
	v_mul_f32_e32 v133, 0xbfb8aa3b, v136
	v_mul_f32_e32 v134, 0xbfb8aa3b, v134
	v_exp_f32_e32 v133, v133
	v_exp_f32_e32 v134, v134
	v_add_f32_e32 v131, 1.0, v131
	v_rcp_f32_e32 v136, v131
	v_add_f32_e32 v131, 1.0, v133
	v_add_f32_e32 v133, 1.0, v134
	v_mul_f32_e32 v134, 0xbfb8aa3b, v137
	v_mul_f32_e32 v132, 0xbfb8aa3b, v132
	v_exp_f32_e32 v134, v134
	v_exp_f32_e32 v132, v132
	v_mul_f32_e32 v135, 0xbfb8aa3b, v135
	v_exp_f32_e32 v135, v135
	v_add_f32_e32 v134, 1.0, v134
	v_add_f32_e32 v132, 1.0, v132
	v_rcp_f32_e32 v130, v130
	v_rcp_f32_e32 v131, v131
	v_rcp_f32_e32 v134, v134
	v_rcp_f32_e32 v132, v132
	v_add_f32_e32 v135, 1.0, v135
	v_cvt_pk_bf16_f32 v130, v132, v130
	v_cvt_pk_bf16_f32 v131, v131, v134
	v_mov_b32_e32 v134, 0x3000
	v_rcp_f32_e32 v133, v133
	v_rcp_f32_e32 v135, v135
	v_lshl_add_u32 v0, v0, 1, v134
	v_cvt_pk_bf16_f32 v132, v138, v136
	v_cvt_pk_bf16_f32 v133, v133, v135
	v_lshl_add_u64 v[134:135], s[10:11], 0, v[0:1]
	flat_store_dwordx4 v[134:135], v[130:133]
	v_pk_mul_f32 v[134:135], v[8:9], v[140:141] op_sel_hi:[1,0]
	v_pk_mul_f32 v[138:139], v[6:7], v[140:141] op_sel_hi:[1,0]
	v_pk_mul_f32 v[136:137], v[4:5], v[140:141] op_sel_hi:[1,0]
	v_pk_mul_f32 v[140:141], v[2:3], v[140:141] op_sel_hi:[1,0]
	s_cbranch_vccnz .LBB0_607
	s_cmp_eq_u64 s[34:35], 0
	s_cbranch_scc1 .Lflg_done
	v_mbcnt_lo_u32_b32 v16, -1, 0
	v_mbcnt_hi_u32_b32 v16, -1, v16
	v_lshrrev_b32_e32 v17, 5, v16
	v_bfe_u32 v16, v16, 4, 1
	v_lshlrev_b32_e32 v17, 9, v17
	v_lshl_add_u32 v17, v16, 7, v17
	v_add_u32_e32 v16, v160, v17
	ds_read_b32 v26, v16
	ds_read_b32 v27, v16 offset:64
	v_lshl_add_u32 v28, v158, 2, v17
	s_mov_b32 s3, 0xbfb8aa3b
	s_mov_b32 s19, 0x3f2aaaab
	s_mov_b32 s21, 0x3f317218
	s_mov_b32 s27, 0x7f800000
	s_mov_b32 s33, 0x33800000
	v_permlane32_swap_b32_e32 v118, v54
	v_permlane32_swap_b32_e32 v119, v55
	v_permlane32_swap_b32_e32 v120, v56
	v_permlane32_swap_b32_e32 v121, v57
	v_permlane32_swap_b32_e32 v114, v50
	v_permlane32_swap_b32_e32 v115, v51
	v_permlane32_swap_b32_e32 v102, v38
	v_permlane32_swap_b32_e32 v103, v39
	v_permlane32_swap_b32_e32 v104, v40
	v_permlane32_swap_b32_e32 v105, v41
	v_permlane32_swap_b32_e32 v98, v34
	v_permlane32_swap_b32_e32 v99, v35
	v_permlane32_swap_b32_e32 v86, v22
	v_permlane32_swap_b32_e32 v87, v23
	v_permlane32_swap_b32_e32 v88, v24
	v_permlane32_swap_b32_e32 v89, v25
	v_permlane32_swap_b32_e32 v82, v18
	v_permlane32_swap_b32_e32 v83, v19
	v_permlane32_swap_b32_e32 v70, v6
	v_permlane32_swap_b32_e32 v71, v7
	v_permlane32_swap_b32_e32 v72, v8
	v_permlane32_swap_b32_e32 v73, v9
	v_permlane32_swap_b32_e32 v66, v2
	v_permlane32_swap_b32_e32 v67, v3
	s_nop 1
	v_permlane16_swap_b32_e32 v118, v86
	v_permlane16_swap_b32_e32 v119, v87
	v_permlane16_swap_b32_e32 v120, v88
	v_permlane16_swap_b32_e32 v121, v89
	v_permlane16_swap_b32_e32 v114, v82
	v_permlane16_swap_b32_e32 v115, v83
	v_permlane16_swap_b32_e32 v102, v70
	v_permlane16_swap_b32_e32 v103, v71
	v_permlane16_swap_b32_e32 v104, v72
	v_permlane16_swap_b32_e32 v105, v73
	v_permlane16_swap_b32_e32 v98, v66
	v_permlane16_swap_b32_e32 v99, v67
	s_waitcnt vmcnt(6) lgkmcnt(0)
	s_nop 1
	v_mul_f32_e32 v118, v118, v26
	v_add_f32_e32 v30, v118, v116
	v_min_f32_e32 v29, 0, v30
	v_mul_f32_e64 v30, |v30|, s3
	v_exp_f32_e32 v30, v30
	s_nop 0
	v_add_f32_e32 v32, 1.0, v30
	v_add_f32_e32 v31, -1.0, v32
	v_sub_f32_e32 v33, v31, v32
	v_add_f32_e32 v33, 1.0, v33
	v_sub_f32_e32 v31, v30, v31
	v_add_f32_e32 v33, v31, v33
	v_frexp_mant_f32_e32 v31, v32
	v_cvt_f64_f32_e32 v[42:43], v32
	v_cmp_gt_f32_e32 vcc, s19, v31
	v_frexp_exp_i32_f64_e32 v31, v[42:43]
	s_nop 0
	v_subbrev_co_u32_e32 v31, vcc, 0, v31, vcc
	v_sub_u32_e32 v42, 0, v31
	v_ldexp_f32 v32, v32, v42
	v_ldexp_f32 v33, v33, v42
	v_add_f32_e32 v42, -1.0, v32
	v_add_f32_e32 v43, 1.0, v42
	v_sub_f32_e32 v43, v32, v43
	v_add_f32_e32 v43, v33, v43
	v_add_f32_e32 v44, v42, v43
	v_sub_f32_e32 v42, v44, v42
	v_sub_f32_e32 v42, v43, v42
	v_add_f32_e32 v43, 1.0, v32
	v_add_f32_e32 v45, -1.0, v43
	v_sub_f32_e32 v32, v32, v45
	v_add_f32_e32 v32, v33, v32
	v_add_f32_e32 v33, v43, v32
	v_sub_f32_e32 v43, v33, v43
	v_sub_f32_e32 v32, v32, v43
	v_rcp_f32_e32 v43, v33
	v_cvt_f32_i32_e32 v31, v31
	v_cmp_neq_f32_e32 vcc, s27, v30
	v_mul_f32_e32 v45, v44, v43
	v_mul_f32_e32 v46, v33, v45
	v_fma_f32 v47, v45, v33, -v46
	v_fmac_f32_e32 v47, v45, v32
	v_add_f32_e32 v48, v46, v47
	v_sub_f32_e32 v49, v44, v48
	v_sub_f32_e32 v44, v44, v49
	v_sub_f32_e32 v46, v48, v46
	v_sub_f32_e32 v44, v44, v48
	v_add_f32_e32 v42, v42, v44
	v_sub_f32_e32 v44, v46, v47
	v_add_f32_e32 v42, v44, v42
	v_add_f32_e32 v44, v49, v42
	v_mul_f32_e32 v46, v43, v44
	v_mul_f32_e32 v47, v33, v46
	v_fma_f32 v33, v46, v33, -v47
	v_fmac_f32_e32 v33, v46, v32
	v_sub_f32_e32 v32, v49, v44
	v_add_f32_e32 v32, v42, v32
	v_add_f32_e32 v42, v47, v33
	v_sub_f32_e32 v48, v44, v42
	v_sub_f32_e32 v44, v44, v48
	v_sub_f32_e32 v47, v42, v47
	v_sub_f32_e32 v42, v44, v42
	v_add_f32_e32 v32, v32, v42
	v_sub_f32_e32 v33, v47, v33
;     __device__ __forceinline__ void operator()(const f32x4 (&acc)[2][2][4][2], const Unit& u, int ui, int wr, int wc, int fr, int fq) const {
;     ...
;                             float z[6] = {y0[0], y0[1], y0[2], y0[3], y1[0], y1[1]};
; #pragma unroll
;                             for (int e = 0; e < 6; ++e) { const float zz = z[e] + bfg[e]; z[e] = fminf(zz, 0.f) - log1pf(__expf(-fabsf(zz))); }
	v_add_f32_e32 v32, v33, v32
	v_add_f32_e32 v33, v45, v46
	v_add_f32_e32 v32, v48, v32
	v_sub_f32_e32 v42, v33, v45
	v_mul_f32_e32 v32, v43, v32
	v_sub_f32_e32 v42, v46, v42
	v_add_f32_e32 v32, v42, v32
	v_mul_f32_e32 v45, 0x3f317218, v31
	v_add_f32_e32 v42, v33, v32
	v_fma_f32 v46, v31, s21, -v45
	v_mul_f32_e32 v43, v42, v42
	v_fmac_f32_e32 v46, 0xb102e308, v31
	v_sub_f32_e32 v31, v42, v33
	v_fmamk_f32 v44, v43, 0x3e9b6dac, v217
	v_sub_f32_e32 v31, v32, v31
	v_add_f32_e32 v32, v45, v46
	v_fmaak_f32 v44, v43, v44, 0x3f2aaada
	v_sub_f32_e32 v33, v32, v45
	v_ldexp_f32 v45, v42, 1
	v_mul_f32_e32 v42, v42, v43
	v_mul_f32_e32 v42, v42, v44
	v_add_f32_e32 v43, v45, v42
	v_sub_f32_e32 v44, v43, v45
	v_ldexp_f32 v31, v31, 1
	v_sub_f32_e32 v42, v42, v44
	v_add_f32_e32 v31, v31, v42
	v_add_f32_e32 v42, v43, v31
	v_sub_f32_e32 v43, v42, v43
	v_sub_f32_e32 v31, v31, v43
	v_add_f32_e32 v43, v32, v42
	v_sub_f32_e32 v44, v43, v32
	v_sub_f32_e32 v45, v43, v44
	v_sub_f32_e32 v33, v46, v33
	v_sub_f32_e32 v32, v32, v45
	v_sub_f32_e32 v42, v42, v44
	v_add_f32_e32 v32, v42, v32
	v_add_f32_e32 v42, v33, v31
	v_sub_f32_e32 v44, v42, v33
	v_sub_f32_e32 v45, v42, v44
	v_sub_f32_e32 v33, v33, v45
	v_sub_f32_e32 v31, v31, v44
	v_add_f32_e32 v32, v42, v32
	v_add_f32_e32 v31, v31, v33
	v_add_f32_e32 v33, v43, v32
	v_sub_f32_e32 v42, v33, v43
	v_sub_f32_e32 v32, v32, v42
	v_add_f32_e32 v31, v31, v32
	v_add_f32_e32 v31, v33, v31
	v_cndmask_b32_e32 v31, v230, v31, vcc
	v_cmp_ngt_f32_e32 vcc, -1.0, v30
	s_nop 1
	v_cndmask_b32_e32 v31, v231, v31, vcc
	v_cmp_neq_f32_e32 vcc, -1.0, v30
	s_nop 1
	v_cndmask_b32_e32 v31, v226, v31, vcc
	v_cmp_lt_f32_e64 vcc, |v30|, s33
	s_nop 1
	v_cndmask_b32_e32 v30, v31, v30, vcc
	v_sub_f32_e32 v118, v29, v30
	v_mul_f32_e32 v119, v119, v26
	v_add_f32_e32 v30, v119, v117
	v_min_f32_e32 v29, 0, v30
	v_mul_f32_e64 v30, |v30|, s3
	v_exp_f32_e32 v30, v30
	s_nop 0
	v_add_f32_e32 v32, 1.0, v30
	v_add_f32_e32 v31, -1.0, v32
	v_sub_f32_e32 v33, v31, v32
	v_add_f32_e32 v33, 1.0, v33
	v_sub_f32_e32 v31, v30, v31
	v_add_f32_e32 v33, v31, v33
	v_frexp_mant_f32_e32 v31, v32
	v_cvt_f64_f32_e32 v[42:43], v32
	v_cmp_gt_f32_e32 vcc, s19, v31
	v_frexp_exp_i32_f64_e32 v31, v[42:43]
	s_nop 0
	v_subbrev_co_u32_e32 v31, vcc, 0, v31, vcc
	v_sub_u32_e32 v42, 0, v31
	v_ldexp_f32 v32, v32, v42
	v_ldexp_f32 v33, v33, v42
	v_add_f32_e32 v42, -1.0, v32
	v_add_f32_e32 v43, 1.0, v42
	v_sub_f32_e32 v43, v32, v43
	v_add_f32_e32 v43, v33, v43
	v_add_f32_e32 v44, v42, v43
	v_sub_f32_e32 v42, v44, v42
	v_sub_f32_e32 v42, v43, v42
	v_add_f32_e32 v43, 1.0, v32
	v_add_f32_e32 v45, -1.0, v43
	v_sub_f32_e32 v32, v32, v45
	v_add_f32_e32 v32, v33, v32
	v_add_f32_e32 v33, v43, v32
	v_sub_f32_e32 v43, v33, v43
	v_sub_f32_e32 v32, v32, v43
	v_rcp_f32_e32 v43, v33
	v_cvt_f32_i32_e32 v31, v31
	v_cmp_neq_f32_e32 vcc, s27, v30
	v_mul_f32_e32 v45, v44, v43
	v_mul_f32_e32 v46, v33, v45
	v_fma_f32 v47, v45, v33, -v46
	v_fmac_f32_e32 v47, v45, v32
	v_add_f32_e32 v48, v46, v47
	v_sub_f32_e32 v49, v44, v48
	v_sub_f32_e32 v44, v44, v49
	v_sub_f32_e32 v46, v48, v46
	v_sub_f32_e32 v44, v44, v48
	v_add_f32_e32 v42, v42, v44
	v_sub_f32_e32 v44, v46, v47
	v_add_f32_e32 v42, v44, v42
	v_add_f32_e32 v44, v49, v42
	v_mul_f32_e32 v46, v43, v44
	v_mul_f32_e32 v47, v33, v46
	v_fma_f32 v33, v46, v33, -v47
	v_fmac_f32_e32 v33, v46, v32
	v_sub_f32_e32 v32, v49, v44
	v_add_f32_e32 v32, v42, v32
	v_add_f32_e32 v42, v47, v33
	v_sub_f32_e32 v48, v44, v42
	v_sub_f32_e32 v44, v44, v48
	v_sub_f32_e32 v47, v42, v47
	v_sub_f32_e32 v42, v44, v42
	v_add_f32_e32 v32, v32, v42
	v_sub_f32_e32 v33, v47, v33
	v_add_f32_e32 v32, v33, v32
	v_add_f32_e32 v33, v45, v46
	v_add_f32_e32 v32, v48, v32
	v_sub_f32_e32 v42, v33, v45
	v_mul_f32_e32 v32, v43, v32
	v_sub_f32_e32 v42, v46, v42
	v_add_f32_e32 v32, v42, v32
	v_mul_f32_e32 v45, 0x3f317218, v31
	v_add_f32_e32 v42, v33, v32
	v_fma_f32 v46, v31, s21, -v45
	v_mul_f32_e32 v43, v42, v42
	v_fmac_f32_e32 v46, 0xb102e308, v31
	v_sub_f32_e32 v31, v42, v33
	v_fmamk_f32 v44, v43, 0x3e9b6dac, v217
	v_sub_f32_e32 v31, v32, v31
	v_add_f32_e32 v32, v45, v46
	v_fmaak_f32 v44, v43, v44, 0x3f2aaada
	v_sub_f32_e32 v33, v32, v45
	v_ldexp_f32 v45, v42, 1
	v_mul_f32_e32 v42, v42, v43
	v_mul_f32_e32 v42, v42, v44
	v_add_f32_e32 v43, v45, v42
	v_sub_f32_e32 v44, v43, v45
	v_ldexp_f32 v31, v31, 1
	v_sub_f32_e32 v42, v42, v44
	v_add_f32_e32 v31, v31, v42
	v_add_f32_e32 v42, v43, v31
	v_sub_f32_e32 v43, v42, v43
	v_sub_f32_e32 v31, v31, v43
	v_add_f32_e32 v43, v32, v42
	v_sub_f32_e32 v44, v43, v32
	v_sub_f32_e32 v45, v43, v44
	v_sub_f32_e32 v33, v46, v33
	v_sub_f32_e32 v32, v32, v45
	v_sub_f32_e32 v42, v42, v44
	v_add_f32_e32 v32, v42, v32
	v_add_f32_e32 v42, v33, v31
	v_sub_f32_e32 v44, v42, v33
	v_sub_f32_e32 v45, v42, v44
	v_sub_f32_e32 v33, v33, v45
	v_sub_f32_e32 v31, v31, v44
	v_add_f32_e32 v32, v42, v32
	v_add_f32_e32 v31, v31, v33
	v_add_f32_e32 v33, v43, v32
	v_sub_f32_e32 v42, v33, v43
	v_sub_f32_e32 v32, v32, v42
	v_add_f32_e32 v31, v31, v32
	v_add_f32_e32 v31, v33, v31
	v_cndmask_b32_e32 v31, v230, v31, vcc
	v_cmp_ngt_f32_e32 vcc, -1.0, v30
	s_nop 1
	v_cndmask_b32_e32 v31, v231, v31, vcc
	v_cmp_neq_f32_e32 vcc, -1.0, v30
	s_nop 1
	v_cndmask_b32_e32 v31, v226, v31, vcc
	v_cmp_lt_f32_e64 vcc, |v30|, s33
	s_nop 1
	v_cndmask_b32_e32 v30, v31, v30, vcc
	v_sub_f32_e32 v119, v29, v30
	v_mul_f32_e32 v120, v120, v26
	v_add_f32_e32 v30, v120, v100
	v_min_f32_e32 v29, 0, v30
	v_mul_f32_e64 v30, |v30|, s3
	v_exp_f32_e32 v30, v30
	s_nop 0
	v_add_f32_e32 v32, 1.0, v30
	v_add_f32_e32 v31, -1.0, v32
	v_sub_f32_e32 v33, v31, v32
	v_add_f32_e32 v33, 1.0, v33
	v_sub_f32_e32 v31, v30, v31
	v_add_f32_e32 v33, v31, v33
;     __device__ __forceinline__ void operator()(const f32x4 (&acc)[2][2][4][2], const Unit& u, int ui, int wr, int wc, int fr, int fq) const {
;     ...
;                             float z[6] = {y0[0], y0[1], y0[2], y0[3], y1[0], y1[1]};
; #pragma unroll
;                             for (int e = 0; e < 6; ++e) { const float zz = z[e] + bfg[e]; z[e] = fminf(zz, 0.f) - log1pf(__expf(-fabsf(zz))); }
	v_frexp_mant_f32_e32 v31, v32
	v_cvt_f64_f32_e32 v[42:43], v32
	v_cmp_gt_f32_e32 vcc, s19, v31
	v_frexp_exp_i32_f64_e32 v31, v[42:43]
	s_nop 0
	v_subbrev_co_u32_e32 v31, vcc, 0, v31, vcc
	v_sub_u32_e32 v42, 0, v31
	v_ldexp_f32 v32, v32, v42
	v_ldexp_f32 v33, v33, v42
	v_add_f32_e32 v42, -1.0, v32
	v_add_f32_e32 v43, 1.0, v42
	v_sub_f32_e32 v43, v32, v43
	v_add_f32_e32 v43, v33, v43
	v_add_f32_e32 v44, v42, v43
	v_sub_f32_e32 v42, v44, v42
	v_sub_f32_e32 v42, v43, v42
	v_add_f32_e32 v43, 1.0, v32
	v_add_f32_e32 v45, -1.0, v43
	v_sub_f32_e32 v32, v32, v45
	v_add_f32_e32 v32, v33, v32
	v_add_f32_e32 v33, v43, v32
	v_sub_f32_e32 v43, v33, v43
	v_sub_f32_e32 v32, v32, v43
	v_rcp_f32_e32 v43, v33
	v_cvt_f32_i32_e32 v31, v31
	v_cmp_neq_f32_e32 vcc, s27, v30
	v_mul_f32_e32 v45, v44, v43
	v_mul_f32_e32 v46, v33, v45
	v_fma_f32 v47, v45, v33, -v46
	v_fmac_f32_e32 v47, v45, v32
	v_add_f32_e32 v48, v46, v47
	v_sub_f32_e32 v49, v44, v48
	v_sub_f32_e32 v44, v44, v49
	v_sub_f32_e32 v46, v48, v46
	v_sub_f32_e32 v44, v44, v48
	v_add_f32_e32 v42, v42, v44
	v_sub_f32_e32 v44, v46, v47
	v_add_f32_e32 v42, v44, v42
	v_add_f32_e32 v44, v49, v42
	v_mul_f32_e32 v46, v43, v44
	v_mul_f32_e32 v47, v33, v46
	v_fma_f32 v33, v46, v33, -v47
	v_fmac_f32_e32 v33, v46, v32
	v_sub_f32_e32 v32, v49, v44
	v_add_f32_e32 v32, v42, v32
	v_add_f32_e32 v42, v47, v33
	v_sub_f32_e32 v48, v44, v42
	v_sub_f32_e32 v44, v44, v48
	v_sub_f32_e32 v47, v42, v47
	v_sub_f32_e32 v42, v44, v42
	v_add_f32_e32 v32, v32, v42
	v_sub_f32_e32 v33, v47, v33
	v_add_f32_e32 v32, v33, v32
	v_add_f32_e32 v33, v45, v46
	v_add_f32_e32 v32, v48, v32
	v_sub_f32_e32 v42, v33, v45
	v_mul_f32_e32 v32, v43, v32
	v_sub_f32_e32 v42, v46, v42
	v_add_f32_e32 v32, v42, v32
	v_mul_f32_e32 v45, 0x3f317218, v31
	v_add_f32_e32 v42, v33, v32
	v_fma_f32 v46, v31, s21, -v45
	v_mul_f32_e32 v43, v42, v42
	v_fmac_f32_e32 v46, 0xb102e308, v31
	v_sub_f32_e32 v31, v42, v33
	v_fmamk_f32 v44, v43, 0x3e9b6dac, v217
	v_sub_f32_e32 v31, v32, v31
	v_add_f32_e32 v32, v45, v46
	v_fmaak_f32 v44, v43, v44, 0x3f2aaada
	v_sub_f32_e32 v33, v32, v45
	v_ldexp_f32 v45, v42, 1
	v_mul_f32_e32 v42, v42, v43
	v_mul_f32_e32 v42, v42, v44
	v_add_f32_e32 v43, v45, v42
	v_sub_f32_e32 v44, v43, v45
	v_ldexp_f32 v31, v31, 1
	v_sub_f32_e32 v42, v42, v44
	v_add_f32_e32 v31, v31, v42
	v_add_f32_e32 v42, v43, v31
	v_sub_f32_e32 v43, v42, v43
	v_sub_f32_e32 v31, v31, v43
	v_add_f32_e32 v43, v32, v42
	v_sub_f32_e32 v44, v43, v32
	v_sub_f32_e32 v45, v43, v44
	v_sub_f32_e32 v33, v46, v33
	v_sub_f32_e32 v32, v32, v45
	v_sub_f32_e32 v42, v42, v44
	v_add_f32_e32 v32, v42, v32
	v_add_f32_e32 v42, v33, v31
	v_sub_f32_e32 v44, v42, v33
	v_sub_f32_e32 v45, v42, v44
	v_sub_f32_e32 v33, v33, v45
	v_sub_f32_e32 v31, v31, v44
	v_add_f32_e32 v32, v42, v32
	v_add_f32_e32 v31, v31, v33
	v_add_f32_e32 v33, v43, v32
	v_sub_f32_e32 v42, v33, v43
	v_sub_f32_e32 v32, v32, v42
	v_add_f32_e32 v31, v31, v32
	v_add_f32_e32 v31, v33, v31
	v_cndmask_b32_e32 v31, v230, v31, vcc
	v_cmp_ngt_f32_e32 vcc, -1.0, v30
	s_nop 1
	v_cndmask_b32_e32 v31, v231, v31, vcc
	v_cmp_neq_f32_e32 vcc, -1.0, v30
	s_nop 1
	v_cndmask_b32_e32 v31, v226, v31, vcc
	v_cmp_lt_f32_e64 vcc, |v30|, s33
	s_nop 1
	v_cndmask_b32_e32 v30, v31, v30, vcc
	v_sub_f32_e32 v120, v29, v30
	v_mul_f32_e32 v121, v121, v26
	v_add_f32_e32 v30, v121, v101
	v_min_f32_e32 v29, 0, v30
	v_mul_f32_e64 v30, |v30|, s3
	v_exp_f32_e32 v30, v30
	s_nop 0
	v_add_f32_e32 v32, 1.0, v30
	v_add_f32_e32 v31, -1.0, v32
	v_sub_f32_e32 v33, v31, v32
	v_add_f32_e32 v33, 1.0, v33
	v_sub_f32_e32 v31, v30, v31
	v_add_f32_e32 v33, v31, v33
	v_frexp_mant_f32_e32 v31, v32
	v_cvt_f64_f32_e32 v[42:43], v32
	v_cmp_gt_f32_e32 vcc, s19, v31
	v_frexp_exp_i32_f64_e32 v31, v[42:43]
	s_nop 0
	v_subbrev_co_u32_e32 v31, vcc, 0, v31, vcc
	v_sub_u32_e32 v42, 0, v31
	v_ldexp_f32 v32, v32, v42
	v_ldexp_f32 v33, v33, v42
	v_add_f32_e32 v42, -1.0, v32
	v_add_f32_e32 v43, 1.0, v42
	v_sub_f32_e32 v43, v32, v43
	v_add_f32_e32 v43, v33, v43
	v_add_f32_e32 v44, v42, v43
	v_sub_f32_e32 v42, v44, v42
	v_sub_f32_e32 v42, v43, v42
	v_add_f32_e32 v43, 1.0, v32
	v_add_f32_e32 v45, -1.0, v43
	v_sub_f32_e32 v32, v32, v45
	v_add_f32_e32 v32, v33, v32
	v_add_f32_e32 v33, v43, v32
	v_sub_f32_e32 v43, v33, v43
	v_sub_f32_e32 v32, v32, v43
	v_rcp_f32_e32 v43, v33
	v_cvt_f32_i32_e32 v31, v31
	v_cmp_neq_f32_e32 vcc, s27, v30
	v_mul_f32_e32 v45, v44, v43
	v_mul_f32_e32 v46, v33, v45
	v_fma_f32 v47, v45, v33, -v46
	v_fmac_f32_e32 v47, v45, v32
	v_add_f32_e32 v48, v46, v47
	v_sub_f32_e32 v49, v44, v48
	v_sub_f32_e32 v44, v44, v49
	v_sub_f32_e32 v46, v48, v46
	v_sub_f32_e32 v44, v44, v48
	v_add_f32_e32 v42, v42, v44
	v_sub_f32_e32 v44, v46, v47
	v_add_f32_e32 v42, v44, v42
	v_add_f32_e32 v44, v49, v42
	v_mul_f32_e32 v46, v43, v44
	v_mul_f32_e32 v47, v33, v46
	v_fma_f32 v33, v46, v33, -v47
	v_fmac_f32_e32 v33, v46, v32
	v_sub_f32_e32 v32, v49, v44
	v_add_f32_e32 v32, v42, v32
	v_add_f32_e32 v42, v47, v33
	v_sub_f32_e32 v48, v44, v42
	v_sub_f32_e32 v44, v44, v48
	v_sub_f32_e32 v47, v42, v47
	v_sub_f32_e32 v42, v44, v42
	v_add_f32_e32 v32, v32, v42
	v_sub_f32_e32 v33, v47, v33
	v_add_f32_e32 v32, v33, v32
	v_add_f32_e32 v33, v45, v46
	v_add_f32_e32 v32, v48, v32
	v_sub_f32_e32 v42, v33, v45
	v_mul_f32_e32 v32, v43, v32
	v_sub_f32_e32 v42, v46, v42
	v_add_f32_e32 v32, v42, v32
	v_mul_f32_e32 v45, 0x3f317218, v31
	v_add_f32_e32 v42, v33, v32
	v_fma_f32 v46, v31, s21, -v45
	v_mul_f32_e32 v43, v42, v42
	v_fmac_f32_e32 v46, 0xb102e308, v31
	v_sub_f32_e32 v31, v42, v33
	v_fmamk_f32 v44, v43, 0x3e9b6dac, v217
	v_sub_f32_e32 v31, v32, v31
	v_add_f32_e32 v32, v45, v46
	v_fmaak_f32 v44, v43, v44, 0x3f2aaada
;     __device__ __forceinline__ void operator()(const f32x4 (&acc)[2][2][4][2], const Unit& u, int ui, int wr, int wc, int fr, int fq) const {
;     ...
;                             float z[6] = {y0[0], y0[1], y0[2], y0[3], y1[0], y1[1]};
; #pragma unroll
;                             for (int e = 0; e < 6; ++e) { const float zz = z[e] + bfg[e]; z[e] = fminf(zz, 0.f) - log1pf(__expf(-fabsf(zz))); }
	v_sub_f32_e32 v33, v32, v45
	v_ldexp_f32 v45, v42, 1
	v_mul_f32_e32 v42, v42, v43
	v_mul_f32_e32 v42, v42, v44
	v_add_f32_e32 v43, v45, v42
	v_sub_f32_e32 v44, v43, v45
	v_ldexp_f32 v31, v31, 1
	v_sub_f32_e32 v42, v42, v44
	v_add_f32_e32 v31, v31, v42
	v_add_f32_e32 v42, v43, v31
	v_sub_f32_e32 v43, v42, v43
	v_sub_f32_e32 v31, v31, v43
	v_add_f32_e32 v43, v32, v42
	v_sub_f32_e32 v44, v43, v32
	v_sub_f32_e32 v45, v43, v44
	v_sub_f32_e32 v33, v46, v33
	v_sub_f32_e32 v32, v32, v45
	v_sub_f32_e32 v42, v42, v44
	v_add_f32_e32 v32, v42, v32
	v_add_f32_e32 v42, v33, v31
	v_sub_f32_e32 v44, v42, v33
	v_sub_f32_e32 v45, v42, v44
	v_sub_f32_e32 v33, v33, v45
	v_sub_f32_e32 v31, v31, v44
	v_add_f32_e32 v32, v42, v32
	v_add_f32_e32 v31, v31, v33
	v_add_f32_e32 v33, v43, v32
	v_sub_f32_e32 v42, v33, v43
	v_sub_f32_e32 v32, v32, v42
	v_add_f32_e32 v31, v31, v32
	v_add_f32_e32 v31, v33, v31
	v_cndmask_b32_e32 v31, v230, v31, vcc
	v_cmp_ngt_f32_e32 vcc, -1.0, v30
	s_nop 1
	v_cndmask_b32_e32 v31, v231, v31, vcc
	v_cmp_neq_f32_e32 vcc, -1.0, v30
	s_nop 1
	v_cndmask_b32_e32 v31, v226, v31, vcc
	v_cmp_lt_f32_e64 vcc, |v30|, s33
	s_nop 1
	v_cndmask_b32_e32 v30, v31, v30, vcc
	v_sub_f32_e32 v121, v29, v30
	v_mul_f32_e32 v114, v114, v26
	v_add_f32_e32 v30, v114, v84
	v_min_f32_e32 v29, 0, v30
	v_mul_f32_e64 v30, |v30|, s3
	v_exp_f32_e32 v30, v30
	s_nop 0
	v_add_f32_e32 v32, 1.0, v30
	v_add_f32_e32 v31, -1.0, v32
	v_sub_f32_e32 v33, v31, v32
	v_add_f32_e32 v33, 1.0, v33
	v_sub_f32_e32 v31, v30, v31
	v_add_f32_e32 v33, v31, v33
	v_frexp_mant_f32_e32 v31, v32
	v_cvt_f64_f32_e32 v[42:43], v32
	v_cmp_gt_f32_e32 vcc, s19, v31
	v_frexp_exp_i32_f64_e32 v31, v[42:43]
	s_nop 0
	v_subbrev_co_u32_e32 v31, vcc, 0, v31, vcc
	v_sub_u32_e32 v42, 0, v31
	v_ldexp_f32 v32, v32, v42
	v_ldexp_f32 v33, v33, v42
	v_add_f32_e32 v42, -1.0, v32
	v_add_f32_e32 v43, 1.0, v42
	v_sub_f32_e32 v43, v32, v43
	v_add_f32_e32 v43, v33, v43
	v_add_f32_e32 v44, v42, v43
	v_sub_f32_e32 v42, v44, v42
	v_sub_f32_e32 v42, v43, v42
	v_add_f32_e32 v43, 1.0, v32
	v_add_f32_e32 v45, -1.0, v43
	v_sub_f32_e32 v32, v32, v45
	v_add_f32_e32 v32, v33, v32
	v_add_f32_e32 v33, v43, v32
	v_sub_f32_e32 v43, v33, v43
	v_sub_f32_e32 v32, v32, v43
	v_rcp_f32_e32 v43, v33
	v_cvt_f32_i32_e32 v31, v31
	v_cmp_neq_f32_e32 vcc, s27, v30
	v_mul_f32_e32 v45, v44, v43
	v_mul_f32_e32 v46, v33, v45
	v_fma_f32 v47, v45, v33, -v46
	v_fmac_f32_e32 v47, v45, v32
	v_add_f32_e32 v48, v46, v47
	v_sub_f32_e32 v49, v44, v48
	v_sub_f32_e32 v44, v44, v49
	v_sub_f32_e32 v46, v48, v46
	v_sub_f32_e32 v44, v44, v48
	v_add_f32_e32 v42, v42, v44
	v_sub_f32_e32 v44, v46, v47
	v_add_f32_e32 v42, v44, v42
	v_add_f32_e32 v44, v49, v42
	v_mul_f32_e32 v46, v43, v44
	v_mul_f32_e32 v47, v33, v46
	v_fma_f32 v33, v46, v33, -v47
	v_fmac_f32_e32 v33, v46, v32
	v_sub_f32_e32 v32, v49, v44
	v_add_f32_e32 v32, v42, v32
	v_add_f32_e32 v42, v47, v33
	v_sub_f32_e32 v48, v44, v42
	v_sub_f32_e32 v44, v44, v48
	v_sub_f32_e32 v47, v42, v47
	v_sub_f32_e32 v42, v44, v42
	v_add_f32_e32 v32, v32, v42
	v_sub_f32_e32 v33, v47, v33
	v_add_f32_e32 v32, v33, v32
	v_add_f32_e32 v33, v45, v46
	v_add_f32_e32 v32, v48, v32
	v_sub_f32_e32 v42, v33, v45
	v_mul_f32_e32 v32, v43, v32
	v_sub_f32_e32 v42, v46, v42
	v_add_f32_e32 v32, v42, v32
	v_mul_f32_e32 v45, 0x3f317218, v31
	v_add_f32_e32 v42, v33, v32
	v_fma_f32 v46, v31, s21, -v45
	v_mul_f32_e32 v43, v42, v42
	v_fmac_f32_e32 v46, 0xb102e308, v31
	v_sub_f32_e32 v31, v42, v33
	v_fmamk_f32 v44, v43, 0x3e9b6dac, v217
	v_sub_f32_e32 v31, v32, v31
	v_add_f32_e32 v32, v45, v46
	v_fmaak_f32 v44, v43, v44, 0x3f2aaada
	v_sub_f32_e32 v33, v32, v45
	v_ldexp_f32 v45, v42, 1
	v_mul_f32_e32 v42, v42, v43
	v_mul_f32_e32 v42, v42, v44
	v_add_f32_e32 v43, v45, v42
	v_sub_f32_e32 v44, v43, v45
	v_ldexp_f32 v31, v31, 1
	v_sub_f32_e32 v42, v42, v44
	v_add_f32_e32 v31, v31, v42
	v_add_f32_e32 v42, v43, v31
	v_sub_f32_e32 v43, v42, v43
	v_sub_f32_e32 v31, v31, v43
	v_add_f32_e32 v43, v32, v42
	v_sub_f32_e32 v44, v43, v32
	v_sub_f32_e32 v45, v43, v44
	v_sub_f32_e32 v33, v46, v33
	v_sub_f32_e32 v32, v32, v45
	v_sub_f32_e32 v42, v42, v44
	v_add_f32_e32 v32, v42, v32
	v_add_f32_e32 v42, v33, v31
	v_sub_f32_e32 v44, v42, v33
	v_sub_f32_e32 v45, v42, v44
	v_sub_f32_e32 v33, v33, v45
	v_sub_f32_e32 v31, v31, v44
	v_add_f32_e32 v32, v42, v32
	v_add_f32_e32 v31, v31, v33
	v_add_f32_e32 v33, v43, v32
	v_sub_f32_e32 v42, v33, v43
	v_sub_f32_e32 v32, v32, v42
	v_add_f32_e32 v31, v31, v32
	v_add_f32_e32 v31, v33, v31
	v_cndmask_b32_e32 v31, v230, v31, vcc
	v_cmp_ngt_f32_e32 vcc, -1.0, v30
	s_nop 1
	v_cndmask_b32_e32 v31, v231, v31, vcc
	v_cmp_neq_f32_e32 vcc, -1.0, v30
	s_nop 1
	v_cndmask_b32_e32 v31, v226, v31, vcc
	v_cmp_lt_f32_e64 vcc, |v30|, s33
	s_nop 1
	v_cndmask_b32_e32 v30, v31, v30, vcc
	v_sub_f32_e32 v114, v29, v30
	v_mul_f32_e32 v115, v115, v26
	v_add_f32_e32 v30, v115, v85
	v_min_f32_e32 v29, 0, v30
	v_mul_f32_e64 v30, |v30|, s3
	v_exp_f32_e32 v30, v30
	s_nop 0
	v_add_f32_e32 v32, 1.0, v30
	v_add_f32_e32 v31, -1.0, v32
	v_sub_f32_e32 v33, v31, v32
	v_add_f32_e32 v33, 1.0, v33
	v_sub_f32_e32 v31, v30, v31
	v_add_f32_e32 v33, v31, v33
	v_frexp_mant_f32_e32 v31, v32
	v_cvt_f64_f32_e32 v[42:43], v32
	v_cmp_gt_f32_e32 vcc, s19, v31
	v_frexp_exp_i32_f64_e32 v31, v[42:43]
	s_nop 0
	v_subbrev_co_u32_e32 v31, vcc, 0, v31, vcc
	v_sub_u32_e32 v42, 0, v31
	v_ldexp_f32 v32, v32, v42
	v_ldexp_f32 v33, v33, v42
	v_add_f32_e32 v42, -1.0, v32
	v_add_f32_e32 v43, 1.0, v42
	v_sub_f32_e32 v43, v32, v43
	v_add_f32_e32 v43, v33, v43
	v_add_f32_e32 v44, v42, v43
	v_sub_f32_e32 v42, v44, v42
	v_sub_f32_e32 v42, v43, v42
	v_add_f32_e32 v43, 1.0, v32
	v_add_f32_e32 v45, -1.0, v43
;     __device__ __forceinline__ void operator()(const f32x4 (&acc)[2][2][4][2], const Unit& u, int ui, int wr, int wc, int fr, int fq) const {
;     ...
;                             float z[6] = {y0[0], y0[1], y0[2], y0[3], y1[0], y1[1]};
; #pragma unroll
;                             for (int e = 0; e < 6; ++e) { const float zz = z[e] + bfg[e]; z[e] = fminf(zz, 0.f) - log1pf(__expf(-fabsf(zz))); }
	v_sub_f32_e32 v32, v32, v45
	v_add_f32_e32 v32, v33, v32
	v_add_f32_e32 v33, v43, v32
	v_sub_f32_e32 v43, v33, v43
	v_sub_f32_e32 v32, v32, v43
	v_rcp_f32_e32 v43, v33
	v_cvt_f32_i32_e32 v31, v31
	v_cmp_neq_f32_e32 vcc, s27, v30
	v_mul_f32_e32 v45, v44, v43
	v_mul_f32_e32 v46, v33, v45
	v_fma_f32 v47, v45, v33, -v46
	v_fmac_f32_e32 v47, v45, v32
	v_add_f32_e32 v48, v46, v47
	v_sub_f32_e32 v49, v44, v48
	v_sub_f32_e32 v44, v44, v49
	v_sub_f32_e32 v46, v48, v46
	v_sub_f32_e32 v44, v44, v48
	v_add_f32_e32 v42, v42, v44
	v_sub_f32_e32 v44, v46, v47
	v_add_f32_e32 v42, v44, v42
	v_add_f32_e32 v44, v49, v42
	v_mul_f32_e32 v46, v43, v44
	v_mul_f32_e32 v47, v33, v46
	v_fma_f32 v33, v46, v33, -v47
	v_fmac_f32_e32 v33, v46, v32
	v_sub_f32_e32 v32, v49, v44
	v_add_f32_e32 v32, v42, v32
	v_add_f32_e32 v42, v47, v33
	v_sub_f32_e32 v48, v44, v42
	v_sub_f32_e32 v44, v44, v48
	v_sub_f32_e32 v47, v42, v47
	v_sub_f32_e32 v42, v44, v42
	v_add_f32_e32 v32, v32, v42
	v_sub_f32_e32 v33, v47, v33
	v_add_f32_e32 v32, v33, v32
	v_add_f32_e32 v33, v45, v46
	v_add_f32_e32 v32, v48, v32
	v_sub_f32_e32 v42, v33, v45
	v_mul_f32_e32 v32, v43, v32
	v_sub_f32_e32 v42, v46, v42
	v_add_f32_e32 v32, v42, v32
	v_mul_f32_e32 v45, 0x3f317218, v31
	v_add_f32_e32 v42, v33, v32
	v_fma_f32 v46, v31, s21, -v45
	v_mul_f32_e32 v43, v42, v42
	v_fmac_f32_e32 v46, 0xb102e308, v31
	v_sub_f32_e32 v31, v42, v33
	v_fmamk_f32 v44, v43, 0x3e9b6dac, v217
	v_sub_f32_e32 v31, v32, v31
	v_add_f32_e32 v32, v45, v46
	v_fmaak_f32 v44, v43, v44, 0x3f2aaada
	v_sub_f32_e32 v33, v32, v45
	v_ldexp_f32 v45, v42, 1
	v_mul_f32_e32 v42, v42, v43
	v_mul_f32_e32 v42, v42, v44
	v_add_f32_e32 v43, v45, v42
	v_sub_f32_e32 v44, v43, v45
	v_ldexp_f32 v31, v31, 1
	v_sub_f32_e32 v42, v42, v44
	v_add_f32_e32 v31, v31, v42
	v_add_f32_e32 v42, v43, v31
	v_sub_f32_e32 v43, v42, v43
	v_sub_f32_e32 v31, v31, v43
	v_add_f32_e32 v43, v32, v42
	v_sub_f32_e32 v44, v43, v32
	v_sub_f32_e32 v45, v43, v44
	v_sub_f32_e32 v33, v46, v33
	v_sub_f32_e32 v32, v32, v45
	v_sub_f32_e32 v42, v42, v44
	v_add_f32_e32 v32, v42, v32
	v_add_f32_e32 v42, v33, v31
	v_sub_f32_e32 v44, v42, v33
	v_sub_f32_e32 v45, v42, v44
	v_sub_f32_e32 v33, v33, v45
	v_sub_f32_e32 v31, v31, v44
	v_add_f32_e32 v32, v42, v32
	v_add_f32_e32 v31, v31, v33
	v_add_f32_e32 v33, v43, v32
	v_sub_f32_e32 v42, v33, v43
	v_sub_f32_e32 v32, v32, v42
	v_add_f32_e32 v31, v31, v32
	v_add_f32_e32 v31, v33, v31
	v_cndmask_b32_e32 v31, v230, v31, vcc
	v_cmp_ngt_f32_e32 vcc, -1.0, v30
	s_nop 1
	v_cndmask_b32_e32 v31, v231, v31, vcc
	v_cmp_neq_f32_e32 vcc, -1.0, v30
	s_nop 1
	v_cndmask_b32_e32 v31, v226, v31, vcc
	v_cmp_lt_f32_e64 vcc, |v30|, s33
	s_nop 1
	v_cndmask_b32_e32 v30, v31, v30, vcc
	v_sub_f32_e32 v115, v29, v30
	v_mul_f32_e32 v102, v102, v27
	v_add_f32_e32 v30, v102, v116
	v_min_f32_e32 v29, 0, v30
	v_mul_f32_e64 v30, |v30|, s3
	v_exp_f32_e32 v30, v30
	s_nop 0
	v_add_f32_e32 v32, 1.0, v30
	v_add_f32_e32 v31, -1.0, v32
	v_sub_f32_e32 v33, v31, v32
	v_add_f32_e32 v33, 1.0, v33
	v_sub_f32_e32 v31, v30, v31
	v_add_f32_e32 v33, v31, v33
	v_frexp_mant_f32_e32 v31, v32
	v_cvt_f64_f32_e32 v[42:43], v32
	v_cmp_gt_f32_e32 vcc, s19, v31
	v_frexp_exp_i32_f64_e32 v31, v[42:43]
	s_nop 0
	v_subbrev_co_u32_e32 v31, vcc, 0, v31, vcc
	v_sub_u32_e32 v42, 0, v31
	v_ldexp_f32 v32, v32, v42
	v_ldexp_f32 v33, v33, v42
	v_add_f32_e32 v42, -1.0, v32
	v_add_f32_e32 v43, 1.0, v42
	v_sub_f32_e32 v43, v32, v43
	v_add_f32_e32 v43, v33, v43
	v_add_f32_e32 v44, v42, v43
	v_sub_f32_e32 v42, v44, v42
	v_sub_f32_e32 v42, v43, v42
	v_add_f32_e32 v43, 1.0, v32
	v_add_f32_e32 v45, -1.0, v43
	v_sub_f32_e32 v32, v32, v45
	v_add_f32_e32 v32, v33, v32
	v_add_f32_e32 v33, v43, v32
	v_sub_f32_e32 v43, v33, v43
	v_sub_f32_e32 v32, v32, v43
	v_rcp_f32_e32 v43, v33
	v_cvt_f32_i32_e32 v31, v31
	v_cmp_neq_f32_e32 vcc, s27, v30
	v_mul_f32_e32 v45, v44, v43
	v_mul_f32_e32 v46, v33, v45
	v_fma_f32 v47, v45, v33, -v46
	v_fmac_f32_e32 v47, v45, v32
	v_add_f32_e32 v48, v46, v47
	v_sub_f32_e32 v49, v44, v48
	v_sub_f32_e32 v44, v44, v49
	v_sub_f32_e32 v46, v48, v46
	v_sub_f32_e32 v44, v44, v48
	v_add_f32_e32 v42, v42, v44
	v_sub_f32_e32 v44, v46, v47
	v_add_f32_e32 v42, v44, v42
	v_add_f32_e32 v44, v49, v42
	v_mul_f32_e32 v46, v43, v44
	v_mul_f32_e32 v47, v33, v46
	v_fma_f32 v33, v46, v33, -v47
	v_fmac_f32_e32 v33, v46, v32
	v_sub_f32_e32 v32, v49, v44
	v_add_f32_e32 v32, v42, v32
	v_add_f32_e32 v42, v47, v33
	v_sub_f32_e32 v48, v44, v42
	v_sub_f32_e32 v44, v44, v48
	v_sub_f32_e32 v47, v42, v47
	v_sub_f32_e32 v42, v44, v42
	v_add_f32_e32 v32, v32, v42
	v_sub_f32_e32 v33, v47, v33
	v_add_f32_e32 v32, v33, v32
	v_add_f32_e32 v33, v45, v46
	v_add_f32_e32 v32, v48, v32
	v_sub_f32_e32 v42, v33, v45
	v_mul_f32_e32 v32, v43, v32
	v_sub_f32_e32 v42, v46, v42
	v_add_f32_e32 v32, v42, v32
	v_mul_f32_e32 v45, 0x3f317218, v31
	v_add_f32_e32 v42, v33, v32
	v_fma_f32 v46, v31, s21, -v45
	v_mul_f32_e32 v43, v42, v42
	v_fmac_f32_e32 v46, 0xb102e308, v31
	v_sub_f32_e32 v31, v42, v33
	v_fmamk_f32 v44, v43, 0x3e9b6dac, v217
	v_sub_f32_e32 v31, v32, v31
	v_add_f32_e32 v32, v45, v46
	v_fmaak_f32 v44, v43, v44, 0x3f2aaada
	v_sub_f32_e32 v33, v32, v45
	v_ldexp_f32 v45, v42, 1
	v_mul_f32_e32 v42, v42, v43
	v_mul_f32_e32 v42, v42, v44
	v_add_f32_e32 v43, v45, v42
	v_sub_f32_e32 v44, v43, v45
	v_ldexp_f32 v31, v31, 1
	v_sub_f32_e32 v42, v42, v44
	v_add_f32_e32 v31, v31, v42
	v_add_f32_e32 v42, v43, v31
	v_sub_f32_e32 v43, v42, v43
	v_sub_f32_e32 v31, v31, v43
	v_add_f32_e32 v43, v32, v42
	v_sub_f32_e32 v44, v43, v32
	v_sub_f32_e32 v45, v43, v44
	v_sub_f32_e32 v33, v46, v33
	v_sub_f32_e32 v32, v32, v45
	v_sub_f32_e32 v42, v42, v44
	v_add_f32_e32 v32, v42, v32
;     __device__ __forceinline__ void operator()(const f32x4 (&acc)[2][2][4][2], const Unit& u, int ui, int wr, int wc, int fr, int fq) const {
;     ...
;                             float z[6] = {y0[0], y0[1], y0[2], y0[3], y1[0], y1[1]};
; #pragma unroll
;                             for (int e = 0; e < 6; ++e) { const float zz = z[e] + bfg[e]; z[e] = fminf(zz, 0.f) - log1pf(__expf(-fabsf(zz))); }
	v_add_f32_e32 v42, v33, v31
	v_sub_f32_e32 v44, v42, v33
	v_sub_f32_e32 v45, v42, v44
	v_sub_f32_e32 v33, v33, v45
	v_sub_f32_e32 v31, v31, v44
	v_add_f32_e32 v32, v42, v32
	v_add_f32_e32 v31, v31, v33
	v_add_f32_e32 v33, v43, v32
	v_sub_f32_e32 v42, v33, v43
	v_sub_f32_e32 v32, v32, v42
	v_add_f32_e32 v31, v31, v32
	v_add_f32_e32 v31, v33, v31
	v_cndmask_b32_e32 v31, v230, v31, vcc
	v_cmp_ngt_f32_e32 vcc, -1.0, v30
	s_nop 1
	v_cndmask_b32_e32 v31, v231, v31, vcc
	v_cmp_neq_f32_e32 vcc, -1.0, v30
	s_nop 1
	v_cndmask_b32_e32 v31, v226, v31, vcc
	v_cmp_lt_f32_e64 vcc, |v30|, s33
	s_nop 1
	v_cndmask_b32_e32 v30, v31, v30, vcc
	v_sub_f32_e32 v102, v29, v30
	v_mul_f32_e32 v103, v103, v27
	v_add_f32_e32 v30, v103, v117
	v_min_f32_e32 v29, 0, v30
	v_mul_f32_e64 v30, |v30|, s3
	v_exp_f32_e32 v30, v30
	s_nop 0
	v_add_f32_e32 v32, 1.0, v30
	v_add_f32_e32 v31, -1.0, v32
	v_sub_f32_e32 v33, v31, v32
	v_add_f32_e32 v33, 1.0, v33
	v_sub_f32_e32 v31, v30, v31
	v_add_f32_e32 v33, v31, v33
	v_frexp_mant_f32_e32 v31, v32
	v_cvt_f64_f32_e32 v[42:43], v32
	v_cmp_gt_f32_e32 vcc, s19, v31
	v_frexp_exp_i32_f64_e32 v31, v[42:43]
	s_nop 0
	v_subbrev_co_u32_e32 v31, vcc, 0, v31, vcc
	v_sub_u32_e32 v42, 0, v31
	v_ldexp_f32 v32, v32, v42
	v_ldexp_f32 v33, v33, v42
	v_add_f32_e32 v42, -1.0, v32
	v_add_f32_e32 v43, 1.0, v42
	v_sub_f32_e32 v43, v32, v43
	v_add_f32_e32 v43, v33, v43
	v_add_f32_e32 v44, v42, v43
	v_sub_f32_e32 v42, v44, v42
	v_sub_f32_e32 v42, v43, v42
	v_add_f32_e32 v43, 1.0, v32
	v_add_f32_e32 v45, -1.0, v43
	v_sub_f32_e32 v32, v32, v45
	v_add_f32_e32 v32, v33, v32
	v_add_f32_e32 v33, v43, v32
	v_sub_f32_e32 v43, v33, v43
	v_sub_f32_e32 v32, v32, v43
	v_rcp_f32_e32 v43, v33
	v_cvt_f32_i32_e32 v31, v31
	v_cmp_neq_f32_e32 vcc, s27, v30
	v_mul_f32_e32 v45, v44, v43
	v_mul_f32_e32 v46, v33, v45
	v_fma_f32 v47, v45, v33, -v46
	v_fmac_f32_e32 v47, v45, v32
	v_add_f32_e32 v48, v46, v47
	v_sub_f32_e32 v49, v44, v48
	v_sub_f32_e32 v44, v44, v49
	v_sub_f32_e32 v46, v48, v46
	v_sub_f32_e32 v44, v44, v48
	v_add_f32_e32 v42, v42, v44
	v_sub_f32_e32 v44, v46, v47
	v_add_f32_e32 v42, v44, v42
	v_add_f32_e32 v44, v49, v42
	v_mul_f32_e32 v46, v43, v44
	v_mul_f32_e32 v47, v33, v46
	v_fma_f32 v33, v46, v33, -v47
	v_fmac_f32_e32 v33, v46, v32
	v_sub_f32_e32 v32, v49, v44
	v_add_f32_e32 v32, v42, v32
	v_add_f32_e32 v42, v47, v33
	v_sub_f32_e32 v48, v44, v42
	v_sub_f32_e32 v44, v44, v48
	v_sub_f32_e32 v47, v42, v47
	v_sub_f32_e32 v42, v44, v42
	v_add_f32_e32 v32, v32, v42
	v_sub_f32_e32 v33, v47, v33
	v_add_f32_e32 v32, v33, v32
	v_add_f32_e32 v33, v45, v46
	v_add_f32_e32 v32, v48, v32
	v_sub_f32_e32 v42, v33, v45
	v_mul_f32_e32 v32, v43, v32
	v_sub_f32_e32 v42, v46, v42
	v_add_f32_e32 v32, v42, v32
	v_mul_f32_e32 v45, 0x3f317218, v31
	v_add_f32_e32 v42, v33, v32
	v_fma_f32 v46, v31, s21, -v45
	v_mul_f32_e32 v43, v42, v42
	v_fmac_f32_e32 v46, 0xb102e308, v31
	v_sub_f32_e32 v31, v42, v33
	v_fmamk_f32 v44, v43, 0x3e9b6dac, v217
	v_sub_f32_e32 v31, v32, v31
	v_add_f32_e32 v32, v45, v46
	v_fmaak_f32 v44, v43, v44, 0x3f2aaada
	v_sub_f32_e32 v33, v32, v45
	v_ldexp_f32 v45, v42, 1
	v_mul_f32_e32 v42, v42, v43
	v_mul_f32_e32 v42, v42, v44
	v_add_f32_e32 v43, v45, v42
	v_sub_f32_e32 v44, v43, v45
	v_ldexp_f32 v31, v31, 1
	v_sub_f32_e32 v42, v42, v44
	v_add_f32_e32 v31, v31, v42
	v_add_f32_e32 v42, v43, v31
	v_sub_f32_e32 v43, v42, v43
	v_sub_f32_e32 v31, v31, v43
	v_add_f32_e32 v43, v32, v42
	v_sub_f32_e32 v44, v43, v32
	v_sub_f32_e32 v45, v43, v44
	v_sub_f32_e32 v33, v46, v33
	v_sub_f32_e32 v32, v32, v45
	v_sub_f32_e32 v42, v42, v44
	v_add_f32_e32 v32, v42, v32
	v_add_f32_e32 v42, v33, v31
	v_sub_f32_e32 v44, v42, v33
	v_sub_f32_e32 v45, v42, v44
	v_sub_f32_e32 v33, v33, v45
	v_sub_f32_e32 v31, v31, v44
	v_add_f32_e32 v32, v42, v32
	v_add_f32_e32 v31, v31, v33
	v_add_f32_e32 v33, v43, v32
	v_sub_f32_e32 v42, v33, v43
	v_sub_f32_e32 v32, v32, v42
	v_add_f32_e32 v31, v31, v32
	v_add_f32_e32 v31, v33, v31
	v_cndmask_b32_e32 v31, v230, v31, vcc
	v_cmp_ngt_f32_e32 vcc, -1.0, v30
	s_nop 1
	v_cndmask_b32_e32 v31, v231, v31, vcc
	v_cmp_neq_f32_e32 vcc, -1.0, v30
	s_nop 1
	v_cndmask_b32_e32 v31, v226, v31, vcc
	v_cmp_lt_f32_e64 vcc, |v30|, s33
	s_nop 1
	v_cndmask_b32_e32 v30, v31, v30, vcc
	v_sub_f32_e32 v103, v29, v30
	v_mul_f32_e32 v104, v104, v27
	v_add_f32_e32 v30, v104, v100
	v_min_f32_e32 v29, 0, v30
	v_mul_f32_e64 v30, |v30|, s3
	v_exp_f32_e32 v30, v30
	s_nop 0
	v_add_f32_e32 v32, 1.0, v30
	v_add_f32_e32 v31, -1.0, v32
	v_sub_f32_e32 v33, v31, v32
	v_add_f32_e32 v33, 1.0, v33
	v_sub_f32_e32 v31, v30, v31
	v_add_f32_e32 v33, v31, v33
	v_frexp_mant_f32_e32 v31, v32
	v_cvt_f64_f32_e32 v[42:43], v32
	v_cmp_gt_f32_e32 vcc, s19, v31
	v_frexp_exp_i32_f64_e32 v31, v[42:43]
	s_nop 0
	v_subbrev_co_u32_e32 v31, vcc, 0, v31, vcc
	v_sub_u32_e32 v42, 0, v31
	v_ldexp_f32 v32, v32, v42
	v_ldexp_f32 v33, v33, v42
	v_add_f32_e32 v42, -1.0, v32
	v_add_f32_e32 v43, 1.0, v42
	v_sub_f32_e32 v43, v32, v43
	v_add_f32_e32 v43, v33, v43
	v_add_f32_e32 v44, v42, v43
	v_sub_f32_e32 v42, v44, v42
	v_sub_f32_e32 v42, v43, v42
	v_add_f32_e32 v43, 1.0, v32
	v_add_f32_e32 v45, -1.0, v43
	v_sub_f32_e32 v32, v32, v45
	v_add_f32_e32 v32, v33, v32
	v_add_f32_e32 v33, v43, v32
	v_sub_f32_e32 v43, v33, v43
	v_sub_f32_e32 v32, v32, v43
	v_rcp_f32_e32 v43, v33
	v_cvt_f32_i32_e32 v31, v31
	v_cmp_neq_f32_e32 vcc, s27, v30
	v_mul_f32_e32 v45, v44, v43
	v_mul_f32_e32 v46, v33, v45
	v_fma_f32 v47, v45, v33, -v46
	v_fmac_f32_e32 v47, v45, v32
	v_add_f32_e32 v48, v46, v47
	v_sub_f32_e32 v49, v44, v48
	v_sub_f32_e32 v44, v44, v49
	v_sub_f32_e32 v46, v48, v46
	v_sub_f32_e32 v44, v44, v48
	v_add_f32_e32 v42, v42, v44
;     __device__ __forceinline__ void operator()(const f32x4 (&acc)[2][2][4][2], const Unit& u, int ui, int wr, int wc, int fr, int fq) const {
;     ...
;                             float z[6] = {y0[0], y0[1], y0[2], y0[3], y1[0], y1[1]};
; #pragma unroll
;                             for (int e = 0; e < 6; ++e) { const float zz = z[e] + bfg[e]; z[e] = fminf(zz, 0.f) - log1pf(__expf(-fabsf(zz))); }
	v_sub_f32_e32 v44, v46, v47
	v_add_f32_e32 v42, v44, v42
	v_add_f32_e32 v44, v49, v42
	v_mul_f32_e32 v46, v43, v44
	v_mul_f32_e32 v47, v33, v46
	v_fma_f32 v33, v46, v33, -v47
	v_fmac_f32_e32 v33, v46, v32
	v_sub_f32_e32 v32, v49, v44
	v_add_f32_e32 v32, v42, v32
	v_add_f32_e32 v42, v47, v33
	v_sub_f32_e32 v48, v44, v42
	v_sub_f32_e32 v44, v44, v48
	v_sub_f32_e32 v47, v42, v47
	v_sub_f32_e32 v42, v44, v42
	v_add_f32_e32 v32, v32, v42
	v_sub_f32_e32 v33, v47, v33
	v_add_f32_e32 v32, v33, v32
	v_add_f32_e32 v33, v45, v46
	v_add_f32_e32 v32, v48, v32
	v_sub_f32_e32 v42, v33, v45
	v_mul_f32_e32 v32, v43, v32
	v_sub_f32_e32 v42, v46, v42
	v_add_f32_e32 v32, v42, v32
	v_mul_f32_e32 v45, 0x3f317218, v31
	v_add_f32_e32 v42, v33, v32
	v_fma_f32 v46, v31, s21, -v45
	v_mul_f32_e32 v43, v42, v42
	v_fmac_f32_e32 v46, 0xb102e308, v31
	v_sub_f32_e32 v31, v42, v33
	v_fmamk_f32 v44, v43, 0x3e9b6dac, v217
	v_sub_f32_e32 v31, v32, v31
	v_add_f32_e32 v32, v45, v46
	v_fmaak_f32 v44, v43, v44, 0x3f2aaada
	v_sub_f32_e32 v33, v32, v45
	v_ldexp_f32 v45, v42, 1
	v_mul_f32_e32 v42, v42, v43
	v_mul_f32_e32 v42, v42, v44
	v_add_f32_e32 v43, v45, v42
	v_sub_f32_e32 v44, v43, v45
	v_ldexp_f32 v31, v31, 1
	v_sub_f32_e32 v42, v42, v44
	v_add_f32_e32 v31, v31, v42
	v_add_f32_e32 v42, v43, v31
	v_sub_f32_e32 v43, v42, v43
	v_sub_f32_e32 v31, v31, v43
	v_add_f32_e32 v43, v32, v42
	v_sub_f32_e32 v44, v43, v32
	v_sub_f32_e32 v45, v43, v44
	v_sub_f32_e32 v33, v46, v33
	v_sub_f32_e32 v32, v32, v45
	v_sub_f32_e32 v42, v42, v44
	v_add_f32_e32 v32, v42, v32
	v_add_f32_e32 v42, v33, v31
	v_sub_f32_e32 v44, v42, v33
	v_sub_f32_e32 v45, v42, v44
	v_sub_f32_e32 v33, v33, v45
	v_sub_f32_e32 v31, v31, v44
	v_add_f32_e32 v32, v42, v32
	v_add_f32_e32 v31, v31, v33
	v_add_f32_e32 v33, v43, v32
	v_sub_f32_e32 v42, v33, v43
	v_sub_f32_e32 v32, v32, v42
	v_add_f32_e32 v31, v31, v32
	v_add_f32_e32 v31, v33, v31
	v_cndmask_b32_e32 v31, v230, v31, vcc
	v_cmp_ngt_f32_e32 vcc, -1.0, v30
	s_nop 1
	v_cndmask_b32_e32 v31, v231, v31, vcc
	v_cmp_neq_f32_e32 vcc, -1.0, v30
	s_nop 1
	v_cndmask_b32_e32 v31, v226, v31, vcc
	v_cmp_lt_f32_e64 vcc, |v30|, s33
	s_nop 1
	v_cndmask_b32_e32 v30, v31, v30, vcc
	v_sub_f32_e32 v104, v29, v30
	v_mul_f32_e32 v105, v105, v27
	v_add_f32_e32 v30, v105, v101
	v_min_f32_e32 v29, 0, v30
	v_mul_f32_e64 v30, |v30|, s3
	v_exp_f32_e32 v30, v30
	s_nop 0
	v_add_f32_e32 v32, 1.0, v30
	v_add_f32_e32 v31, -1.0, v32
	v_sub_f32_e32 v33, v31, v32
	v_add_f32_e32 v33, 1.0, v33
	v_sub_f32_e32 v31, v30, v31
	v_add_f32_e32 v33, v31, v33
	v_frexp_mant_f32_e32 v31, v32
	v_cvt_f64_f32_e32 v[42:43], v32
	v_cmp_gt_f32_e32 vcc, s19, v31
	v_frexp_exp_i32_f64_e32 v31, v[42:43]
	s_nop 0
	v_subbrev_co_u32_e32 v31, vcc, 0, v31, vcc
	v_sub_u32_e32 v42, 0, v31
	v_ldexp_f32 v32, v32, v42
	v_ldexp_f32 v33, v33, v42
	v_add_f32_e32 v42, -1.0, v32
	v_add_f32_e32 v43, 1.0, v42
	v_sub_f32_e32 v43, v32, v43
	v_add_f32_e32 v43, v33, v43
	v_add_f32_e32 v44, v42, v43
	v_sub_f32_e32 v42, v44, v42
	v_sub_f32_e32 v42, v43, v42
	v_add_f32_e32 v43, 1.0, v32
	v_add_f32_e32 v45, -1.0, v43
	v_sub_f32_e32 v32, v32, v45
	v_add_f32_e32 v32, v33, v32
	v_add_f32_e32 v33, v43, v32
	v_sub_f32_e32 v43, v33, v43
	v_sub_f32_e32 v32, v32, v43
	v_rcp_f32_e32 v43, v33
	v_cvt_f32_i32_e32 v31, v31
	v_cmp_neq_f32_e32 vcc, s27, v30
	v_mul_f32_e32 v45, v44, v43
	v_mul_f32_e32 v46, v33, v45
	v_fma_f32 v47, v45, v33, -v46
	v_fmac_f32_e32 v47, v45, v32
	v_add_f32_e32 v48, v46, v47
	v_sub_f32_e32 v49, v44, v48
	v_sub_f32_e32 v44, v44, v49
	v_sub_f32_e32 v46, v48, v46
	v_sub_f32_e32 v44, v44, v48
	v_add_f32_e32 v42, v42, v44
	v_sub_f32_e32 v44, v46, v47
	v_add_f32_e32 v42, v44, v42
	v_add_f32_e32 v44, v49, v42
	v_mul_f32_e32 v46, v43, v44
	v_mul_f32_e32 v47, v33, v46
	v_fma_f32 v33, v46, v33, -v47
	v_fmac_f32_e32 v33, v46, v32
	v_sub_f32_e32 v32, v49, v44
	v_add_f32_e32 v32, v42, v32
	v_add_f32_e32 v42, v47, v33
	v_sub_f32_e32 v48, v44, v42
	v_sub_f32_e32 v44, v44, v48
	v_sub_f32_e32 v47, v42, v47
	v_sub_f32_e32 v42, v44, v42
	v_add_f32_e32 v32, v32, v42
	v_sub_f32_e32 v33, v47, v33
	v_add_f32_e32 v32, v33, v32
	v_add_f32_e32 v33, v45, v46
	v_add_f32_e32 v32, v48, v32
	v_sub_f32_e32 v42, v33, v45
	v_mul_f32_e32 v32, v43, v32
	v_sub_f32_e32 v42, v46, v42
	v_add_f32_e32 v32, v42, v32
	v_mul_f32_e32 v45, 0x3f317218, v31
	v_add_f32_e32 v42, v33, v32
	v_fma_f32 v46, v31, s21, -v45
	v_mul_f32_e32 v43, v42, v42
	v_fmac_f32_e32 v46, 0xb102e308, v31
	v_sub_f32_e32 v31, v42, v33
	v_fmamk_f32 v44, v43, 0x3e9b6dac, v217
	v_sub_f32_e32 v31, v32, v31
	v_add_f32_e32 v32, v45, v46
	v_fmaak_f32 v44, v43, v44, 0x3f2aaada
	v_sub_f32_e32 v33, v32, v45
	v_ldexp_f32 v45, v42, 1
	v_mul_f32_e32 v42, v42, v43
	v_mul_f32_e32 v42, v42, v44
	v_add_f32_e32 v43, v45, v42
	v_sub_f32_e32 v44, v43, v45
	v_ldexp_f32 v31, v31, 1
	v_sub_f32_e32 v42, v42, v44
	v_add_f32_e32 v31, v31, v42
	v_add_f32_e32 v42, v43, v31
	v_sub_f32_e32 v43, v42, v43
	v_sub_f32_e32 v31, v31, v43
	v_add_f32_e32 v43, v32, v42
	v_sub_f32_e32 v44, v43, v32
	v_sub_f32_e32 v45, v43, v44
	v_sub_f32_e32 v33, v46, v33
	v_sub_f32_e32 v32, v32, v45
	v_sub_f32_e32 v42, v42, v44
	v_add_f32_e32 v32, v42, v32
	v_add_f32_e32 v42, v33, v31
	v_sub_f32_e32 v44, v42, v33
	v_sub_f32_e32 v45, v42, v44
	v_sub_f32_e32 v33, v33, v45
	v_sub_f32_e32 v31, v31, v44
	v_add_f32_e32 v32, v42, v32
	v_add_f32_e32 v31, v31, v33
	v_add_f32_e32 v33, v43, v32
	v_sub_f32_e32 v42, v33, v43
	v_sub_f32_e32 v32, v32, v42
	v_add_f32_e32 v31, v31, v32
	v_add_f32_e32 v31, v33, v31
	v_cndmask_b32_e32 v31, v230, v31, vcc
	v_cmp_ngt_f32_e32 vcc, -1.0, v30
	s_nop 1
	v_cndmask_b32_e32 v31, v231, v31, vcc
	v_cmp_neq_f32_e32 vcc, -1.0, v30
	s_nop 1
;     __device__ __forceinline__ void operator()(const f32x4 (&acc)[2][2][4][2], const Unit& u, int ui, int wr, int wc, int fr, int fq) const {
;     ...
;                             float z[6] = {y0[0], y0[1], y0[2], y0[3], y1[0], y1[1]};
; #pragma unroll
;                             for (int e = 0; e < 6; ++e) { const float zz = z[e] + bfg[e]; z[e] = fminf(zz, 0.f) - log1pf(__expf(-fabsf(zz))); }
	v_cndmask_b32_e32 v31, v226, v31, vcc
	v_cmp_lt_f32_e64 vcc, |v30|, s33
	s_nop 1
	v_cndmask_b32_e32 v30, v31, v30, vcc
	v_sub_f32_e32 v105, v29, v30
	v_mul_f32_e32 v98, v98, v27
	v_add_f32_e32 v30, v98, v84
	v_min_f32_e32 v29, 0, v30
	v_mul_f32_e64 v30, |v30|, s3
	v_exp_f32_e32 v30, v30
	s_nop 0
	v_add_f32_e32 v32, 1.0, v30
	v_add_f32_e32 v31, -1.0, v32
	v_sub_f32_e32 v33, v31, v32
	v_add_f32_e32 v33, 1.0, v33
	v_sub_f32_e32 v31, v30, v31
	v_add_f32_e32 v33, v31, v33
	v_frexp_mant_f32_e32 v31, v32
	v_cvt_f64_f32_e32 v[42:43], v32
	v_cmp_gt_f32_e32 vcc, s19, v31
	v_frexp_exp_i32_f64_e32 v31, v[42:43]
	s_nop 0
	v_subbrev_co_u32_e32 v31, vcc, 0, v31, vcc
	v_sub_u32_e32 v42, 0, v31
	v_ldexp_f32 v32, v32, v42
	v_ldexp_f32 v33, v33, v42
	v_add_f32_e32 v42, -1.0, v32
	v_add_f32_e32 v43, 1.0, v42
	v_sub_f32_e32 v43, v32, v43
	v_add_f32_e32 v43, v33, v43
	v_add_f32_e32 v44, v42, v43
	v_sub_f32_e32 v42, v44, v42
	v_sub_f32_e32 v42, v43, v42
	v_add_f32_e32 v43, 1.0, v32
	v_add_f32_e32 v45, -1.0, v43
	v_sub_f32_e32 v32, v32, v45
	v_add_f32_e32 v32, v33, v32
	v_add_f32_e32 v33, v43, v32
	v_sub_f32_e32 v43, v33, v43
	v_sub_f32_e32 v32, v32, v43
	v_rcp_f32_e32 v43, v33
	v_cvt_f32_i32_e32 v31, v31
	v_cmp_neq_f32_e32 vcc, s27, v30
	v_mul_f32_e32 v45, v44, v43
	v_mul_f32_e32 v46, v33, v45
	v_fma_f32 v47, v45, v33, -v46
	v_fmac_f32_e32 v47, v45, v32
	v_add_f32_e32 v48, v46, v47
	v_sub_f32_e32 v49, v44, v48
	v_sub_f32_e32 v44, v44, v49
	v_sub_f32_e32 v46, v48, v46
	v_sub_f32_e32 v44, v44, v48
	v_add_f32_e32 v42, v42, v44
	v_sub_f32_e32 v44, v46, v47
	v_add_f32_e32 v42, v44, v42
	v_add_f32_e32 v44, v49, v42
	v_mul_f32_e32 v46, v43, v44
	v_mul_f32_e32 v47, v33, v46
	v_fma_f32 v33, v46, v33, -v47
	v_fmac_f32_e32 v33, v46, v32
	v_sub_f32_e32 v32, v49, v44
	v_add_f32_e32 v32, v42, v32
	v_add_f32_e32 v42, v47, v33
	v_sub_f32_e32 v48, v44, v42
	v_sub_f32_e32 v44, v44, v48
	v_sub_f32_e32 v47, v42, v47
	v_sub_f32_e32 v42, v44, v42
	v_add_f32_e32 v32, v32, v42
	v_sub_f32_e32 v33, v47, v33
	v_add_f32_e32 v32, v33, v32
	v_add_f32_e32 v33, v45, v46
	v_add_f32_e32 v32, v48, v32
	v_sub_f32_e32 v42, v33, v45
	v_mul_f32_e32 v32, v43, v32
	v_sub_f32_e32 v42, v46, v42
	v_add_f32_e32 v32, v42, v32
	v_mul_f32_e32 v45, 0x3f317218, v31
	v_add_f32_e32 v42, v33, v32
	v_fma_f32 v46, v31, s21, -v45
	v_mul_f32_e32 v43, v42, v42
	v_fmac_f32_e32 v46, 0xb102e308, v31
	v_sub_f32_e32 v31, v42, v33
	v_fmamk_f32 v44, v43, 0x3e9b6dac, v217
	v_sub_f32_e32 v31, v32, v31
	v_add_f32_e32 v32, v45, v46
	v_fmaak_f32 v44, v43, v44, 0x3f2aaada
	v_sub_f32_e32 v33, v32, v45
	v_ldexp_f32 v45, v42, 1
	v_mul_f32_e32 v42, v42, v43
	v_mul_f32_e32 v42, v42, v44
	v_add_f32_e32 v43, v45, v42
	v_sub_f32_e32 v44, v43, v45
	v_ldexp_f32 v31, v31, 1
	v_sub_f32_e32 v42, v42, v44
	v_add_f32_e32 v31, v31, v42
	v_add_f32_e32 v42, v43, v31
	v_sub_f32_e32 v43, v42, v43
	v_sub_f32_e32 v31, v31, v43
	v_add_f32_e32 v43, v32, v42
	v_sub_f32_e32 v44, v43, v32
	v_sub_f32_e32 v45, v43, v44
	v_sub_f32_e32 v33, v46, v33
	v_sub_f32_e32 v32, v32, v45
	v_sub_f32_e32 v42, v42, v44
	v_add_f32_e32 v32, v42, v32
	v_add_f32_e32 v42, v33, v31
	v_sub_f32_e32 v44, v42, v33
	v_sub_f32_e32 v45, v42, v44
	v_sub_f32_e32 v33, v33, v45
	v_sub_f32_e32 v31, v31, v44
	v_add_f32_e32 v32, v42, v32
	v_add_f32_e32 v31, v31, v33
	v_add_f32_e32 v33, v43, v32
	v_sub_f32_e32 v42, v33, v43
	v_sub_f32_e32 v32, v32, v42
	v_add_f32_e32 v31, v31, v32
	v_add_f32_e32 v31, v33, v31
	v_cndmask_b32_e32 v31, v230, v31, vcc
	v_cmp_ngt_f32_e32 vcc, -1.0, v30
	s_nop 1
	v_cndmask_b32_e32 v31, v231, v31, vcc
	v_cmp_neq_f32_e32 vcc, -1.0, v30
	s_nop 1
	v_cndmask_b32_e32 v31, v226, v31, vcc
	v_cmp_lt_f32_e64 vcc, |v30|, s33
	s_nop 1
	v_cndmask_b32_e32 v30, v31, v30, vcc
	v_sub_f32_e32 v98, v29, v30
	v_mul_f32_e32 v99, v99, v27
	v_add_f32_e32 v30, v99, v85
	v_min_f32_e32 v29, 0, v30
	v_mul_f32_e64 v30, |v30|, s3
	v_exp_f32_e32 v30, v30
	s_nop 0
	v_add_f32_e32 v32, 1.0, v30
	v_add_f32_e32 v31, -1.0, v32
	v_sub_f32_e32 v33, v31, v32
	v_add_f32_e32 v33, 1.0, v33
	v_sub_f32_e32 v31, v30, v31
	v_add_f32_e32 v33, v31, v33
	v_frexp_mant_f32_e32 v31, v32
;     __device__ __forceinline__ void operator()(const f32x4 (&acc)[2][2][4][2], const Unit& u, int ui, int wr, int wc, int fr, int fq) const {
;     ...
;                             float z[6] = {y0[0], y0[1], y0[2], y0[3], y1[0], y1[1]};
; #pragma unroll
;                             for (int e = 0; e < 6; ++e) { const float zz = z[e] + bfg[e]; z[e] = fminf(zz, 0.f) - log1pf(__expf(-fabsf(zz))); }
;                             float* lp = (float*)(ws + E_LS) + (size_t)row;
; #pragma unroll
;                             for (int e = 0; e < 6; ++e) lp[(size_t)(e * 32768u)] = z[e];
	v_cvt_f64_f32_e32 v[42:43], v32
	v_cmp_gt_f32_e32 vcc, s19, v31
	v_frexp_exp_i32_f64_e32 v31, v[42:43]
	s_nop 0
	v_subbrev_co_u32_e32 v31, vcc, 0, v31, vcc
	v_sub_u32_e32 v42, 0, v31
	v_ldexp_f32 v32, v32, v42
	v_ldexp_f32 v33, v33, v42
	v_add_f32_e32 v42, -1.0, v32
	v_add_f32_e32 v43, 1.0, v42
	v_sub_f32_e32 v43, v32, v43
	v_add_f32_e32 v43, v33, v43
	v_add_f32_e32 v44, v42, v43
	v_sub_f32_e32 v42, v44, v42
	v_sub_f32_e32 v42, v43, v42
	v_add_f32_e32 v43, 1.0, v32
	v_add_f32_e32 v45, -1.0, v43
	v_sub_f32_e32 v32, v32, v45
	v_add_f32_e32 v32, v33, v32
	v_add_f32_e32 v33, v43, v32
	v_sub_f32_e32 v43, v33, v43
	v_sub_f32_e32 v32, v32, v43
	v_rcp_f32_e32 v43, v33
	v_cvt_f32_i32_e32 v31, v31
	v_cmp_neq_f32_e32 vcc, s27, v30
	v_mul_f32_e32 v45, v44, v43
	v_mul_f32_e32 v46, v33, v45
	v_fma_f32 v47, v45, v33, -v46
	v_fmac_f32_e32 v47, v45, v32
	v_add_f32_e32 v48, v46, v47
	v_sub_f32_e32 v49, v44, v48
	v_sub_f32_e32 v44, v44, v49
	v_sub_f32_e32 v46, v48, v46
	v_sub_f32_e32 v44, v44, v48
	v_add_f32_e32 v42, v42, v44
	v_sub_f32_e32 v44, v46, v47
	v_add_f32_e32 v42, v44, v42
	v_add_f32_e32 v44, v49, v42
	v_mul_f32_e32 v46, v43, v44
	v_mul_f32_e32 v47, v33, v46
	v_fma_f32 v33, v46, v33, -v47
	v_fmac_f32_e32 v33, v46, v32
	v_sub_f32_e32 v32, v49, v44
	v_add_f32_e32 v32, v42, v32
	v_add_f32_e32 v42, v47, v33
	v_sub_f32_e32 v48, v44, v42
	v_sub_f32_e32 v44, v44, v48
	v_sub_f32_e32 v47, v42, v47
	v_sub_f32_e32 v42, v44, v42
	v_add_f32_e32 v32, v32, v42
	v_sub_f32_e32 v33, v47, v33
	v_add_f32_e32 v32, v33, v32
	v_add_f32_e32 v33, v45, v46
	v_add_f32_e32 v32, v48, v32
	v_sub_f32_e32 v42, v33, v45
	v_mul_f32_e32 v32, v43, v32
	v_sub_f32_e32 v42, v46, v42
	v_add_f32_e32 v32, v42, v32
	v_mul_f32_e32 v45, 0x3f317218, v31
	v_add_f32_e32 v42, v33, v32
	v_fma_f32 v46, v31, s21, -v45
	v_mul_f32_e32 v43, v42, v42
	v_fmac_f32_e32 v46, 0xb102e308, v31
	v_sub_f32_e32 v31, v42, v33
	v_fmamk_f32 v44, v43, 0x3e9b6dac, v217
	v_sub_f32_e32 v31, v32, v31
	v_add_f32_e32 v32, v45, v46
	v_fmaak_f32 v44, v43, v44, 0x3f2aaada
	v_sub_f32_e32 v33, v32, v45
	v_ldexp_f32 v45, v42, 1
	v_mul_f32_e32 v42, v42, v43
	v_mul_f32_e32 v42, v42, v44
	v_add_f32_e32 v43, v45, v42
	v_sub_f32_e32 v44, v43, v45
	v_ldexp_f32 v31, v31, 1
	v_sub_f32_e32 v42, v42, v44
	v_add_f32_e32 v31, v31, v42
	v_add_f32_e32 v42, v43, v31
	v_sub_f32_e32 v43, v42, v43
	v_sub_f32_e32 v31, v31, v43
	v_add_f32_e32 v43, v32, v42
	v_sub_f32_e32 v44, v43, v32
	v_sub_f32_e32 v45, v43, v44
	v_sub_f32_e32 v33, v46, v33
	v_sub_f32_e32 v32, v32, v45
	v_sub_f32_e32 v42, v42, v44
	v_add_f32_e32 v32, v42, v32
	v_add_f32_e32 v42, v33, v31
	v_sub_f32_e32 v44, v42, v33
	v_sub_f32_e32 v45, v42, v44
	v_sub_f32_e32 v33, v33, v45
	v_sub_f32_e32 v31, v31, v44
	v_add_f32_e32 v32, v42, v32
	v_add_f32_e32 v31, v31, v33
	v_add_f32_e32 v33, v43, v32
	v_sub_f32_e32 v42, v33, v43
	v_sub_f32_e32 v32, v32, v42
	v_add_f32_e32 v31, v31, v32
	v_add_f32_e32 v31, v33, v31
	v_cndmask_b32_e32 v31, v230, v31, vcc
	v_cmp_ngt_f32_e32 vcc, -1.0, v30
	s_nop 1
	v_cndmask_b32_e32 v31, v231, v31, vcc
	v_cmp_neq_f32_e32 vcc, -1.0, v30
	s_nop 1
	v_cndmask_b32_e32 v31, v226, v31, vcc
	v_cmp_lt_f32_e64 vcc, |v30|, s33
	s_nop 1
	v_cndmask_b32_e32 v30, v31, v30, vcc
	v_sub_f32_e32 v99, v29, v30
	s_mov_b64 s[30:31], s[12:13]
	global_store_dword v28, v118, s[30:31]
	global_store_dword v28, v102, s[30:31] offset:64
	s_add_u32 s30, s30, 0x20000
	s_addc_u32 s31, s31, 0
	global_store_dword v28, v119, s[30:31]
	global_store_dword v28, v103, s[30:31] offset:64
	s_add_u32 s30, s30, 0x20000
	s_addc_u32 s31, s31, 0
	global_store_dword v28, v120, s[30:31]
	global_store_dword v28, v104, s[30:31] offset:64
	s_add_u32 s30, s30, 0x20000
	s_addc_u32 s31, s31, 0
	global_store_dword v28, v121, s[30:31]
	global_store_dword v28, v105, s[30:31] offset:64
	s_add_u32 s30, s30, 0x20000
	s_addc_u32 s31, s31, 0
	global_store_dword v28, v114, s[30:31]
	global_store_dword v28, v98, s[30:31] offset:64
	s_add_u32 s30, s30, 0x20000
	s_addc_u32 s31, s31, 0
	global_store_dword v28, v115, s[30:31]
	global_store_dword v28, v99, s[30:31] offset:64
